# u14 + runs of lgkmcnt waits merged into one (30 fewer s_waitcnt per iteration pair)
# speedup vs baseline: 1.0150x; 1.0150x over previous
; template <bool FIRST> DEVI bool partialSM(f32x16& p0, f32x16& p1, float& m_reg, float& alpha) {
;     float pmax = p0[0];
; #pragma unroll
;     for (int r = 1; r < 16; ++r) pmax = fmaxf(pmax, p0[r]);
; #pragma unroll
;     for (int r = 0; r < 16; ++r) pmax = fmaxf(pmax, p1[r]);
;     { auto rr = __builtin_amdgcn_permlane32_swap(__float_as_uint(pmax), __float_as_uint(pmax), false, false);
;       pmax = fmaxf(__uint_as_float(rr[0]), __uint_as_float(rr[1])); }
;     if (FIRST) { m_reg = pmax; alpha = 1.f;
; #pragma unroll
;         for (int r = 0; r < 16; ++r) { p0[r] = __builtin_amdgcn_exp2f(p0[r] - pmax); p1[r] = p1[r] - pmax; }
;         return false;
;     } else if (__builtin_expect(__all(pmax <= ATT_THR), 1)) { alpha = 1.f;
; #pragma unroll
;         for (int r = 0; r < 16; ++r) p0[r] = __builtin_amdgcn_exp2f(p0[r]);
;         return false;
;     } else { const float d = fmaxf(pmax, 0.f); alpha = __builtin_amdgcn_exp2f(-d); m_reg += d;
; #pragma unroll
;         for (int r = 0; r < 16; ++r) { p0[r] = __builtin_amdgcn_exp2f(p0[r] - d); p1[r] = p1[r] - d; }
;         return true;
;     }
; }
; DEVI void finishSM(f32x16& p0, f32x16& p1, float alpha, float& l_reg, bf16x8& pa0, bf16x8& pa1, bf16x8& pa2, bf16x8& pa3) {
; #pragma unroll
;     for (int r = 0; r < 16; ++r) p1[r] = __builtin_amdgcn_exp2f(p1[r]);
;     f32x2 s2 = (f32x2){p0[0], p0[1]} + (f32x2){p1[0], p1[1]};
; #pragma unroll
;     for (int r = 2; r < 16; r += 2) s2 += (f32x2){p0[r], p0[r + 1]} + (f32x2){p1[r], p1[r + 1]};
;     float ps = s2[0] + s2[1];
;     { auto rr = __builtin_amdgcn_permlane32_swap(__float_as_uint(ps), __float_as_uint(ps), false, false);
;       ps = __uint_as_float(rr[0]) + __uint_as_float(rr[1]); }
;     l_reg = l_reg * alpha + ps;
;     ...
;     PK4(p0, 0, pa0); PK4(p0, 8, pa1); PK4(p1, 0, pa2); PK4(p1, 8, pa3);
;     ...
; }
; DEVI void qkt(f32x16& p0, f32x16& p1, const char* Kb, const bf16x8 (&qr)[6], int r32, int hi, const f32x16& cinit) {
; #pragma unroll
;     for (int d0 = 0; d0 < 6; ++d0) { const int cb = (d0 * 16 + hi * 8) * 2;
;         const bf16x8 k0 = *(const bf16x8*)(Kb + KSWZ(r32, cb)), k1 = *(const bf16x8*)(Kb + KSWZ(32 + r32, cb));
;         p0 = __builtin_amdgcn_mfma_f32_32x32x16_bf16(k0, qr[d0], d0 == 0 ? cinit : p0, 0, 0, 0);
;         p1 = __builtin_amdgcn_mfma_f32_32x32x16_bf16(k1, qr[d0], d0 == 0 ? cinit : p1, 0, 0, 0); }
; }
.LBB0_696:
	v_add_u32_e32 v174, s98, v204
	v_exp_f32_e32 v66, v66
	v_exp_f32_e32 v67, v67
	s_waitcnt lgkmcnt(1)
	v_mfma_f32_32x32x16_bf16 v[98:113], v[82:85], v[150:153], v[34:49]
	v_add_u32_e32 v82, s98, v184
	v_add_u32_e32 v83, s98, v185
	ds_read_b128 v[208:211], v82 offset:12288
	ds_read_b128 v[212:215], v82 offset:18432
	ds_read_b128 v[216:219], v83 offset:12288
	ds_read_b128 v[220:223], v83 offset:18432
	v_exp_f32_e32 v68, v68
	v_exp_f32_e32 v69, v69
	v_exp_f32_e32 v70, v70
	v_exp_f32_e32 v71, v71
	s_waitcnt lgkmcnt(4)
	v_mfma_f32_32x32x16_bf16 v[82:97], v[124:127], v[150:153], v[34:49]
	ds_read_b128 v[124:127], v174 offset:12288
	ds_read_b128 v[224:227], v174 offset:18432
	v_exp_f32_e32 v72, v72
	v_exp_f32_e32 v73, v73
	v_exp_f32_e32 v74, v74
	v_exp_f32_e32 v75, v75
	v_exp_f32_e32 v76, v76
	v_exp_f32_e32 v77, v77
	s_waitcnt lgkmcnt(5)
	v_mfma_f32_32x32x16_bf16 v[98:113], v[208:211], v[138:141], v[98:113]
	v_add_u32_e32 v174, s98, v205
	v_exp_f32_e32 v78, v78
	v_exp_f32_e32 v79, v79
	ds_read_b128 v[228:231], v174 offset:12288
	ds_read_b128 v[232:235], v174 offset:18432
	v_exp_f32_e32 v80, v80
	v_exp_f32_e32 v81, v81
	v_add_u32_e32 v174, s98, v206
	s_waitcnt lgkmcnt(6)
	v_mfma_f32_32x32x16_bf16 v[82:97], v[212:215], v[138:141], v[82:97]
	v_add_f32_e64 v212, v50, v66
	v_add_f32_e64 v213, v51, v67
	v_add_f32_e64 v214, v52, v68
	v_add_f32_e64 v215, v53, v69
	v_lshl_add_u32 v202, s89, 14, v115
	v_add_f32_e32 v212, v214, v212
	v_add_f32_e32 v213, v215, v213
	v_add_f32_e32 v214, v54, v70
	v_add_f32_e32 v215, v55, v71
	ds_read_b128 v[208:211], v174 offset:12288
	ds_read_b128 v[236:239], v174 offset:18432
	v_add_f32_e32 v212, v214, v212
	v_add_f32_e32 v213, v215, v213
	s_waitcnt lgkmcnt(4)
	v_mfma_f32_32x32x16_bf16 v[98:113], v[216:219], v[134:137], v[98:113]
	v_add_f32_e64 v214, v56, v72
	v_add_f32_e64 v215, v57, v73
	v_cvt_pk_bf16_f32 v50, v50, v51
	v_cvt_pk_bf16_f32 v51, v52, v53
	v_cvt_pk_bf16_f32 v52, v54, v55
	v_cvt_pk_bf16_f32 v53, v56, v57
	v_cvt_pk_bf16_f32 v54, v58, v59
	v_add_f32_e64 v212, v214, v212
	v_add_f32_e64 v213, v215, v213
	v_mfma_f32_32x32x16_bf16 v[82:97], v[220:223], v[134:137], v[82:97]
	v_add_f32_e64 v214, v58, v74
	v_add_f32_e64 v215, v59, v75
	v_cvt_pk_bf16_f32 v55, v60, v61
	v_cvt_pk_bf16_f32 v56, v62, v63
	v_cvt_pk_bf16_f32 v57, v64, v65
	v_cvt_pk_bf16_f32 v58, v66, v67
	v_cvt_pk_bf16_f32 v59, v68, v69
	v_add_f32_e64 v212, v214, v212
	v_add_f32_e64 v213, v215, v213
	v_mfma_f32_32x32x16_bf16 v[98:113], v[124:127], v[130:133], v[98:113]
	v_add_f32_e64 v214, v60, v76
	v_add_f32_e64 v215, v61, v77
	v_add_f32_e64 v126, v62, v78
	v_add_f32_e64 v127, v63, v79
	v_add_f32_e64 v124, v214, v212
	v_add_f32_e64 v125, v215, v213
	v_cvt_pk_bf16_f32 v60, v70, v71
	v_cvt_pk_bf16_f32 v61, v72, v73
	v_cvt_pk_bf16_f32 v62, v74, v75
	v_cvt_pk_bf16_f32 v63, v76, v77
	v_mfma_f32_32x32x16_bf16 v[82:97], v[224:227], v[130:133], v[82:97]
	v_add_f32_e64 v124, v126, v124
	v_add_f32_e64 v125, v127, v125
	v_add_f32_e64 v126, v64, v80
	v_add_f32_e64 v127, v65, v81
	v_cvt_pk_bf16_f32 v64, v78, v79
	v_cvt_pk_bf16_f32 v65, v80, v81
	ds_read_b64_tr_b16 v[66:67], v202 offset:0
	ds_read_b64_tr_b16 v[68:69], v202 offset:0x400
	ds_read_b64_tr_b16 v[70:71], v202 offset:0x800
	s_waitcnt lgkmcnt(6)
	v_mfma_f32_32x32x16_bf16 v[98:113], v[228:231], v[146:149], v[98:113]
	ds_read_b64_tr_b16 v[72:73], v202 offset:0xc00
	ds_read_b64_tr_b16 v[74:75], v202 offset:0x1000
	ds_read_b64_tr_b16 v[76:77], v202 offset:0x1400
	ds_read_b64_tr_b16 v[78:79], v202 offset:0x1800
	ds_read_b64_tr_b16 v[80:81], v202 offset:0x1c00
	v_add_f32_e64 v124, v126, v124
	v_add_f32_e64 v125, v127, v125
	s_waitcnt lgkmcnt(9)
	v_mfma_f32_32x32x16_bf16 v[82:97], v[232:235], v[146:149], v[82:97]
	v_add_f32_e32 v124, v124, v125
	s_nop 0
	v_mov_b32_e32 v125, v124
	s_nop 1
	v_permlane32_swap_b32_e32 v124, v125
	v_mfma_f32_32x32x16_bf16 v[98:113], v[208:211], v[142:145], v[98:113]
	ds_read_b64_tr_b16 v[208:209], v202 offset:0x200
	ds_read_b64_tr_b16 v[210:211], v202 offset:0x600
	ds_read_b64_tr_b16 v[212:213], v202 offset:0xa00
	ds_read_b64_tr_b16 v[214:215], v202 offset:0xe00
	ds_read_b64_tr_b16 v[216:217], v202 offset:0x1200
	ds_read_b64_tr_b16 v[218:219], v202 offset:0x1600
	ds_read_b64_tr_b16 v[220:221], v202 offset:0x1a00
	s_waitcnt lgkmcnt(15)
	v_mfma_f32_32x32x16_bf16 v[82:97], v[236:239], v[142:145], v[82:97]
	ds_read_b64_tr_b16 v[222:223], v202 offset:0x1e00
	s_waitcnt lgkmcnt(4)
	v_mfma_f32_32x32x16_bf16 v[18:33], v[50:53], v[66:69], v[18:33]
	v_mfma_f32_32x32x16_bf16 v[2:17], v[50:53], v[208:211], v[2:17]
	s_nop 8
	v_max_f32_e32 v249, v99, v99
	v_max_f32_e32 v250, v98, v98
	v_max_f32_e32 v249, v250, v249
	v_max3_f32 v249, v249, v100, v101
	v_max3_f32 v249, v249, v102, v103
	v_max3_f32 v251, v249, v104, v105
	v_max3_f32 v251, v251, v106, v107
	v_exp_f32_e32 v50, v98
	v_exp_f32_e32 v51, v99
	v_exp_f32_e32 v52, v100
	v_exp_f32_e32 v53, v101
	v_mfma_f32_32x32x16_bf16 v[18:33], v[54:57], v[70:73], v[18:33]
	v_mfma_f32_32x32x16_bf16 v[2:17], v[54:57], v[212:215], v[2:17]
	v_max3_f32 v251, v251, v108, v109
	v_max3_f32 v251, v251, v110, v111
	v_max3_f32 v251, v251, v112, v113
	v_max3_f32 v251, v251, v82, v83
	v_max3_f32 v251, v251, v84, v85
	v_max3_f32 v251, v251, v86, v87
	v_max3_f32 v251, v251, v88, v89
	v_exp_f32_e32 v54, v102
	v_exp_f32_e32 v55, v103
	v_exp_f32_e32 v56, v104
	v_exp_f32_e32 v57, v105
	v_mfma_f32_32x32x16_bf16 v[18:33], v[58:61], v[74:77], v[18:33]
	s_waitcnt lgkmcnt(0)
	v_mfma_f32_32x32x16_bf16 v[2:17], v[58:61], v[216:219], v[2:17]
	v_max3_f32 v251, v251, v90, v91
	v_max3_f32 v251, v251, v92, v93
	v_max3_f32 v251, v251, v94, v95
	v_max3_f32 v251, v251, v96, v97
	v_mov_b32_e32 v252, v251
	s_nop 1
	v_permlane32_swap_b32_e32 v251, v252
	v_exp_f32_e32 v58, v106
	v_exp_f32_e32 v59, v107
	v_exp_f32_e32 v60, v108
	v_exp_f32_e32 v61, v109
	v_mfma_f32_32x32x16_bf16 v[18:33], v[62:65], v[78:81], v[18:33]
	v_mfma_f32_32x32x16_bf16 v[2:17], v[62:65], v[220:223], v[2:17]
	v_exp_f32_e32 v62, v110
	v_exp_f32_e32 v63, v111
	v_exp_f32_e32 v64, v112
	v_exp_f32_e32 v65, v113
	v_max_f32_e32 v252, v252, v252
	v_max_f32_e32 v251, v251, v251
	v_max_f32_e32 v126, v251, v252
	v_cmp_ge_f32_e32 vcc, s79, v126
	s_cmp_lg_u64 vcc, exec
	s_cselect_b64 s[6:7], -1, 0
	s_cbranch_scc1 .LBB0_705
	v_mov_b32_e32 v208, 1.0
	v_mov_b32_e32 v209, v203
	s_branch .LBB0_699

; template <bool FIRST> DEVI bool partialSM(f32x16& p0, f32x16& p1, float& m_reg, float& alpha) {
;     float pmax = p0[0];
; #pragma unroll
;     for (int r = 1; r < 16; ++r) pmax = fmaxf(pmax, p0[r]);
; #pragma unroll
;     for (int r = 0; r < 16; ++r) pmax = fmaxf(pmax, p1[r]);
;     { auto rr = __builtin_amdgcn_permlane32_swap(__float_as_uint(pmax), __float_as_uint(pmax), false, false);
;       pmax = fmaxf(__uint_as_float(rr[0]), __uint_as_float(rr[1])); }
;     if (FIRST) { m_reg = pmax; alpha = 1.f;
; #pragma unroll
;         for (int r = 0; r < 16; ++r) { p0[r] = __builtin_amdgcn_exp2f(p0[r] - pmax); p1[r] = p1[r] - pmax; }
;         return false;
;     } else if (__builtin_expect(__all(pmax <= ATT_THR), 1)) { alpha = 1.f;
; #pragma unroll
;         for (int r = 0; r < 16; ++r) p0[r] = __builtin_amdgcn_exp2f(p0[r]);
;         return false;
;     } else { const float d = fmaxf(pmax, 0.f); alpha = __builtin_amdgcn_exp2f(-d); m_reg += d;
; #pragma unroll
;         for (int r = 0; r < 16; ++r) { p0[r] = __builtin_amdgcn_exp2f(p0[r] - d); p1[r] = p1[r] - d; }
;         return true;
;     }
; }
; DEVI void finishSM(f32x16& p0, f32x16& p1, float alpha, float& l_reg, bf16x8& pa0, bf16x8& pa1, bf16x8& pa2, bf16x8& pa3) {
; #pragma unroll
;     for (int r = 0; r < 16; ++r) p1[r] = __builtin_amdgcn_exp2f(p1[r]);
;     f32x2 s2 = (f32x2){p0[0], p0[1]} + (f32x2){p1[0], p1[1]};
; #pragma unroll
;     for (int r = 2; r < 16; r += 2) s2 += (f32x2){p0[r], p0[r + 1]} + (f32x2){p1[r], p1[r + 1]};
;     float ps = s2[0] + s2[1];
;     { auto rr = __builtin_amdgcn_permlane32_swap(__float_as_uint(ps), __float_as_uint(ps), false, false);
;       ps = __uint_as_float(rr[0]) + __uint_as_float(rr[1]); }
;     l_reg = l_reg * alpha + ps;
;     ...
;     PK4(p0, 0, pa0); PK4(p0, 8, pa1); PK4(p1, 0, pa2); PK4(p1, 8, pa3);
;     ...
; }
; DEVI void qkt(f32x16& p0, f32x16& p1, const char* Kb, const bf16x8 (&qr)[6], int r32, int hi, const f32x16& cinit) {
; #pragma unroll
;     for (int d0 = 0; d0 < 6; ++d0) { const int cb = (d0 * 16 + hi * 8) * 2;
;         const bf16x8 k0 = *(const bf16x8*)(Kb + KSWZ(r32, cb)), k1 = *(const bf16x8*)(Kb + KSWZ(32 + r32, cb));
;         p0 = __builtin_amdgcn_mfma_f32_32x32x16_bf16(k0, qr[d0], d0 == 0 ? cinit : p0, 0, 0, 0);
;         p1 = __builtin_amdgcn_mfma_f32_32x32x16_bf16(k1, qr[d0], d0 == 0 ? cinit : p1, 0, 0, 0); }
; }
.LBB0_702:
	s_mul_i32 s98, s2, 0x6000
	s_add_i32 s98, s96, s98
	s_lshl_b32 s99, s2, 14
	s_add_i32 s99, s97, s99
	s_mul_i32 s6, s61, 0x6000
	s_add_i32 s6, s6, 0
	v_add_u32_e32 v249, s6, v129
	v_lshl_add_u64 v[250:251], v[118:119], 0, s[12:13]
	s_mov_b32 m0, s98
	s_barrier
	ds_read_b128 v[234:237], v249
	ds_read_b128 v[210:213], v249 offset:6144
	global_load_lds_dwordx4 v[250:251], off
	v_exp_f32_e32 v82, v82
	s_waitcnt lgkmcnt(0)
	v_mfma_f32_32x32x16_bf16 v[98:113], v[234:237], v[150:153], v[34:49]
	v_add_u32_e32 v126, s6, v184
	v_lshl_add_u64 v[250:251], v[120:121], 0, s[12:13]
	s_add_i32 m0, s98, 0x2000
	v_exp_f32_e32 v83, v83
	v_exp_f32_e32 v84, v84
	global_load_lds_dwordx4 v[250:251], off
	v_exp_f32_e32 v85, v85
	v_exp_f32_e32 v86, v86
	v_exp_f32_e32 v87, v87
	v_exp_f32_e32 v88, v88
	v_mfma_f32_32x32x16_bf16 v[66:81], v[210:213], v[150:153], v[34:49]
	ds_read_b128 v[210:213], v126
	ds_read_b128 v[214:217], v126 offset:6144
	v_add_u32_e32 v126, s6, v185
	v_lshl_add_u64 v[250:251], v[122:123], 0, s[12:13]
	s_add_i32 m0, s98, 0x4000
	v_exp_f32_e32 v89, v89
	v_exp_f32_e32 v90, v90
	global_load_lds_dwordx4 v[250:251], off
	v_exp_f32_e32 v91, v91
	v_exp_f32_e32 v92, v92
	v_exp_f32_e32 v93, v93
	s_waitcnt lgkmcnt(0)
	v_mfma_f32_32x32x16_bf16 v[98:113], v[210:213], v[138:141], v[98:113]
	s_mov_b32 m0, s99
	v_exp_f32_e32 v94, v94
	v_exp_f32_e32 v95, v95
	v_lshl_add_u64 v[250:251], v[116:117], 0, s[40:41]
	global_load_lds_dwordx4 v[116:117], off
	s_add_i32 m0, s99, 0x2000
	v_exp_f32_e32 v96, v96
	v_exp_f32_e32 v97, v97
	v_add_u32_e32 v174, 0x2000, v202
	global_load_lds_dwordx4 v[250:251], off
	v_mfma_f32_32x32x16_bf16 v[66:81], v[214:217], v[138:141], v[66:81]
	ds_read_b128 v[210:213], v126
	ds_read_b128 v[214:217], v126 offset:6144
	v_add_u32_e32 v126, s6, v204
	s_waitcnt lgkmcnt(1)
	v_mfma_f32_32x32x16_bf16 v[98:113], v[210:213], v[134:137], v[98:113]
	ds_read_b128 v[210:213], v126
	ds_read_b128 v[218:221], v126 offset:6144
	v_add_u32_e32 v126, s6, v205
	s_waitcnt lgkmcnt(2)
	v_mfma_f32_32x32x16_bf16 v[66:81], v[214:217], v[134:137], v[66:81]
	ds_read_b128 v[214:217], v126
	ds_read_b128 v[222:225], v126 offset:6144
	v_add_u32_e32 v126, s6, v206
	ds_read_b128 v[226:229], v126
	ds_read_b128 v[230:233], v126 offset:6144
	v_add_f32_e32 v126, v50, v82
	v_add_f32_e32 v127, v51, v83
	v_cvt_pk_bf16_f32 v50, v50, v51
	v_cvt_pk_bf16_f32 v51, v52, v53
	s_waitcnt lgkmcnt(2)
	v_mfma_f32_32x32x16_bf16 v[98:113], v[210:213], v[130:133], v[98:113]
	v_add_f32_e64 v210, v52, v84
	v_add_f32_e64 v211, v53, v85
	v_cvt_pk_bf16_f32 v52, v54, v55
	v_cvt_pk_bf16_f32 v53, v56, v57
	v_add_f32_e64 v126, v210, v126
	v_add_f32_e64 v127, v211, v127
	v_add_f32_e64 v210, v54, v86
	v_add_f32_e64 v211, v55, v87
	v_cvt_pk_bf16_f32 v54, v58, v59
	v_mfma_f32_32x32x16_bf16 v[66:81], v[218:221], v[130:133], v[66:81]
	v_add_f32_e64 v126, v210, v126
	v_add_f32_e64 v127, v211, v127
	v_add_f32_e64 v210, v56, v88
	v_add_f32_e64 v211, v57, v89
	v_cvt_pk_bf16_f32 v55, v60, v61
	v_cvt_pk_bf16_f32 v56, v62, v63
	v_cvt_pk_bf16_f32 v57, v64, v65
	v_add_f32_e64 v126, v210, v126
	v_add_f32_e64 v127, v211, v127
	v_add_f32_e32 v210, v58, v90
	v_add_f32_e32 v211, v59, v91
	v_cvt_pk_bf16_f32 v58, v82, v83
	v_cvt_pk_bf16_f32 v59, v84, v85
	v_mfma_f32_32x32x16_bf16 v[98:113], v[214:217], v[146:149], v[98:113]
	v_add_f32_e64 v126, v210, v126
	v_add_f32_e64 v127, v211, v127
	v_add_f32_e64 v210, v60, v92
	v_add_f32_e64 v211, v61, v93
	v_cvt_pk_bf16_f32 v60, v86, v87
	v_cvt_pk_bf16_f32 v61, v88, v89
	v_add_f32_e64 v126, v210, v126
	v_add_f32_e64 v127, v211, v127
	v_add_f32_e32 v210, v62, v94
	v_add_f32_e32 v211, v63, v95
	v_cvt_pk_bf16_f32 v62, v90, v91
	v_cvt_pk_bf16_f32 v63, v92, v93
	v_mfma_f32_32x32x16_bf16 v[66:81], v[222:225], v[146:149], v[66:81]
	v_add_f32_e64 v126, v210, v126
	v_add_f32_e64 v127, v211, v127
	v_add_f32_e64 v210, v64, v96
	v_add_f32_e64 v211, v65, v97
	v_cvt_pk_bf16_f32 v64, v94, v95
	v_cvt_pk_bf16_f32 v65, v96, v97
	ds_read_b64_tr_b16 v[154:155], v174 offset:0
	ds_read_b64_tr_b16 v[156:157], v174 offset:0x400
	ds_read_b64_tr_b16 v[158:159], v174 offset:0x800
	ds_read_b64_tr_b16 v[160:161], v174 offset:0xc00
	ds_read_b64_tr_b16 v[162:163], v174 offset:0x1000
	ds_read_b64_tr_b16 v[164:165], v174 offset:0x1400
	ds_read_b64_tr_b16 v[166:167], v174 offset:0x1800
	ds_read_b64_tr_b16 v[168:169], v174 offset:0x1c00
	v_add_f32_e64 v126, v210, v126
	v_add_f32_e64 v127, v211, v127
	ds_read_b64_tr_b16 v[210:211], v174 offset:0x200
	ds_read_b64_tr_b16 v[212:213], v174 offset:0x600
	ds_read_b64_tr_b16 v[214:215], v174 offset:0xa00
	s_waitcnt lgkmcnt(12)
	v_mfma_f32_32x32x16_bf16 v[98:113], v[226:229], v[142:145], v[98:113]
	ds_read_b64_tr_b16 v[216:217], v174 offset:0xe00
	ds_read_b64_tr_b16 v[218:219], v174 offset:0x1200
	ds_read_b64_tr_b16 v[220:221], v174 offset:0x1600
	ds_read_b64_tr_b16 v[222:223], v174 offset:0x1a00
	ds_read_b64_tr_b16 v[224:225], v174 offset:0x1e00
	v_add_f32_e32 v126, v126, v127
	s_waitcnt lgkmcnt(6)
	v_mfma_f32_32x32x16_bf16 v[66:81], v[230:233], v[142:145], v[66:81]
	v_mov_b32_e32 v127, v126
	s_nop 1
	v_permlane32_swap_b32_e32 v126, v127
	v_mfma_f32_32x32x16_bf16 v[18:33], v[50:53], v[154:157], v[18:33]
	v_mfma_f32_32x32x16_bf16 v[2:17], v[50:53], v[210:213], v[2:17]
	s_nop 4
	v_max_f32_e32 v249, v99, v99
	v_max_f32_e32 v250, v98, v98
	v_max_f32_e32 v249, v250, v249
	v_max3_f32 v249, v249, v100, v101
	v_max3_f32 v249, v249, v102, v103
	v_max3_f32 v251, v249, v104, v105
	v_max3_f32 v251, v251, v106, v107
	v_exp_f32_e32 v50, v98
	v_exp_f32_e32 v51, v99
	v_exp_f32_e32 v52, v100
	v_exp_f32_e32 v53, v101
	v_mfma_f32_32x32x16_bf16 v[18:33], v[54:57], v[158:161], v[18:33]
	s_waitcnt lgkmcnt(2)
	v_mfma_f32_32x32x16_bf16 v[2:17], v[54:57], v[214:217], v[2:17]
	v_max3_f32 v251, v251, v108, v109
	v_max3_f32 v251, v251, v110, v111
	v_max3_f32 v251, v251, v112, v113
	v_max3_f32 v251, v251, v66, v67
	v_max3_f32 v251, v251, v68, v69
	v_max3_f32 v251, v251, v70, v71
	v_max3_f32 v251, v251, v72, v73
	v_exp_f32_e32 v54, v102
	v_exp_f32_e32 v55, v103
	v_exp_f32_e32 v56, v104
	v_exp_f32_e32 v57, v105
	v_mfma_f32_32x32x16_bf16 v[18:33], v[58:61], v[162:165], v[18:33]
	v_mfma_f32_32x32x16_bf16 v[2:17], v[58:61], v[218:221], v[2:17]
	v_max3_f32 v251, v251, v74, v75
	v_max3_f32 v251, v251, v76, v77
	v_max3_f32 v251, v251, v78, v79
	v_max3_f32 v251, v251, v80, v81
	v_mov_b32_e32 v252, v251
	s_nop 1
	v_permlane32_swap_b32_e32 v251, v252
	v_exp_f32_e32 v58, v106
	v_exp_f32_e32 v59, v107
	v_exp_f32_e32 v60, v108
	v_exp_f32_e32 v61, v109
	v_mfma_f32_32x32x16_bf16 v[18:33], v[62:65], v[166:169], v[18:33]
	s_waitcnt lgkmcnt(0)
	v_mfma_f32_32x32x16_bf16 v[2:17], v[62:65], v[222:225], v[2:17]
	v_exp_f32_e32 v62, v110
	v_exp_f32_e32 v63, v111
	v_exp_f32_e32 v64, v112
	v_exp_f32_e32 v65, v113
	v_max_f32_e32 v252, v252, v252
	v_max_f32_e32 v251, v251, v251
	v_max_f32_e32 v174, v251, v252
	v_cmp_ge_f32_e32 vcc, s79, v174
	s_cmp_lg_u64 vcc, exec
	s_cselect_b64 s[6:7], -1, 0
	s_cbranch_scc1 .LBB0_711
	v_mov_b32_e32 v202, 1.0
	v_mov_b32_e32 v203, v209
	s_branch .LBB0_716

; template <bool FIRST> DEVI bool partialSM(f32x16& p0, f32x16& p1, float& m_reg, float& alpha) {
;     float pmax = p0[0];
; #pragma unroll
;     for (int r = 1; r < 16; ++r) pmax = fmaxf(pmax, p0[r]);
; #pragma unroll
;     for (int r = 0; r < 16; ++r) pmax = fmaxf(pmax, p1[r]);
;     { auto rr = __builtin_amdgcn_permlane32_swap(__float_as_uint(pmax), __float_as_uint(pmax), false, false);
;       pmax = fmaxf(__uint_as_float(rr[0]), __uint_as_float(rr[1])); }
;     if (FIRST) { m_reg = pmax; alpha = 1.f;
; #pragma unroll
;         for (int r = 0; r < 16; ++r) { p0[r] = __builtin_amdgcn_exp2f(p0[r] - pmax); p1[r] = p1[r] - pmax; }
;         return false;
;     } else if (__builtin_expect(__all(pmax <= ATT_THR), 1)) { alpha = 1.f;
; #pragma unroll
;         for (int r = 0; r < 16; ++r) p0[r] = __builtin_amdgcn_exp2f(p0[r]);
;         return false;
;     } else { const float d = fmaxf(pmax, 0.f); alpha = __builtin_amdgcn_exp2f(-d); m_reg += d;
; #pragma unroll
;         for (int r = 0; r < 16; ++r) { p0[r] = __builtin_amdgcn_exp2f(p0[r] - d); p1[r] = p1[r] - d; }
;         return true;
;     }
; }
; DEVI void finishSM(f32x16& p0, f32x16& p1, float alpha, float& l_reg, bf16x8& pa0, bf16x8& pa1, bf16x8& pa2, bf16x8& pa3) {
; #pragma unroll
;     for (int r = 0; r < 16; ++r) p1[r] = __builtin_amdgcn_exp2f(p1[r]);
;     f32x2 s2 = (f32x2){p0[0], p0[1]} + (f32x2){p1[0], p1[1]};
; #pragma unroll
;     for (int r = 2; r < 16; r += 2) s2 += (f32x2){p0[r], p0[r + 1]} + (f32x2){p1[r], p1[r + 1]};
;     float ps = s2[0] + s2[1];
;     { auto rr = __builtin_amdgcn_permlane32_swap(__float_as_uint(ps), __float_as_uint(ps), false, false);
;       ps = __uint_as_float(rr[0]) + __uint_as_float(rr[1]); }
;     l_reg = l_reg * alpha + ps;
;     ...
;     PK4(p0, 0, pa0); PK4(p0, 8, pa1); PK4(p1, 0, pa2); PK4(p1, 8, pa3);
;     ...
; }
; DEVI void qkt(f32x16& p0, f32x16& p1, const char* Kb, const bf16x8 (&qr)[6], int r32, int hi, const f32x16& cinit) {
; #pragma unroll
;     for (int d0 = 0; d0 < 6; ++d0) { const int cb = (d0 * 16 + hi * 8) * 2;
;         const bf16x8 k0 = *(const bf16x8*)(Kb + KSWZ(r32, cb)), k1 = *(const bf16x8*)(Kb + KSWZ(32 + r32, cb));
;         p0 = __builtin_amdgcn_mfma_f32_32x32x16_bf16(k0, qr[d0], d0 == 0 ? cinit : p0, 0, 0, 0);
;         p1 = __builtin_amdgcn_mfma_f32_32x32x16_bf16(k1, qr[d0], d0 == 0 ? cinit : p1, 0, 0, 0); }
; }
.LBB0_2260:
	v_add_u32_e32 v174, s98, v205
	v_exp_f32_e32 v66, v66
	v_exp_f32_e32 v67, v67
	s_waitcnt lgkmcnt(1)
	v_mfma_f32_32x32x16_bf16 v[98:113], v[82:85], v[150:153], v[34:49]
	v_add_u32_e32 v82, s98, v184
	v_add_u32_e32 v83, s98, v185
	ds_read_b128 v[210:213], v82 offset:12288
	ds_read_b128 v[214:217], v82 offset:18432
	ds_read_b128 v[218:221], v83 offset:12288
	ds_read_b128 v[222:225], v83 offset:18432
	v_exp_f32_e32 v68, v68
	v_exp_f32_e32 v69, v69
	v_exp_f32_e32 v70, v70
	v_exp_f32_e32 v71, v71
	s_waitcnt lgkmcnt(4)
	v_mfma_f32_32x32x16_bf16 v[82:97], v[124:127], v[150:153], v[34:49]
	ds_read_b128 v[124:127], v174 offset:12288
	ds_read_b128 v[226:229], v174 offset:18432
	v_exp_f32_e32 v72, v72
	v_exp_f32_e32 v73, v73
	v_exp_f32_e32 v74, v74
	v_exp_f32_e32 v75, v75
	v_exp_f32_e32 v76, v76
	v_exp_f32_e32 v77, v77
	s_waitcnt lgkmcnt(5)
	v_mfma_f32_32x32x16_bf16 v[98:113], v[210:213], v[138:141], v[98:113]
	v_add_u32_e32 v174, s98, v206
	v_exp_f32_e32 v78, v78
	v_exp_f32_e32 v79, v79
	ds_read_b128 v[230:233], v174 offset:12288
	ds_read_b128 v[234:237], v174 offset:18432
	v_exp_f32_e32 v80, v80
	v_exp_f32_e32 v81, v81
	v_add_u32_e32 v174, s98, v207
	s_waitcnt lgkmcnt(6)
	v_mfma_f32_32x32x16_bf16 v[82:97], v[214:217], v[138:141], v[82:97]
	v_add_f32_e64 v214, v50, v66
	v_add_f32_e64 v215, v51, v67
	v_add_f32_e64 v216, v52, v68
	v_add_f32_e64 v217, v53, v69
	v_lshl_add_u32 v203, s71, 14, v115
	v_add_f32_e32 v214, v216, v214
	v_add_f32_e32 v215, v217, v215
	v_add_f32_e32 v216, v54, v70
	v_add_f32_e32 v217, v55, v71
	ds_read_b128 v[210:213], v174 offset:12288
	ds_read_b128 v[238:241], v174 offset:18432
	v_add_f32_e32 v214, v216, v214
	v_add_f32_e32 v215, v217, v215
	s_waitcnt lgkmcnt(4)
	v_mfma_f32_32x32x16_bf16 v[98:113], v[218:221], v[134:137], v[98:113]
	v_add_f32_e64 v216, v56, v72
	v_add_f32_e64 v217, v57, v73
	v_cvt_pk_bf16_f32 v50, v50, v51
	v_cvt_pk_bf16_f32 v51, v52, v53
	v_cvt_pk_bf16_f32 v52, v54, v55
	v_cvt_pk_bf16_f32 v53, v56, v57
	v_cvt_pk_bf16_f32 v54, v58, v59
	v_add_f32_e64 v214, v216, v214
	v_add_f32_e64 v215, v217, v215
	v_mfma_f32_32x32x16_bf16 v[82:97], v[222:225], v[134:137], v[82:97]
	v_add_f32_e64 v216, v58, v74
	v_add_f32_e64 v217, v59, v75
	v_cvt_pk_bf16_f32 v55, v60, v61
	v_cvt_pk_bf16_f32 v56, v62, v63
	v_cvt_pk_bf16_f32 v57, v64, v65
	v_cvt_pk_bf16_f32 v58, v66, v67
	v_cvt_pk_bf16_f32 v59, v68, v69
	v_add_f32_e64 v214, v216, v214
	v_add_f32_e64 v215, v217, v215
	v_mfma_f32_32x32x16_bf16 v[98:113], v[124:127], v[130:133], v[98:113]
	v_add_f32_e64 v216, v60, v76
	v_add_f32_e64 v217, v61, v77
	v_add_f32_e64 v126, v62, v78
	v_add_f32_e64 v127, v63, v79
	v_add_f32_e64 v124, v216, v214
	v_add_f32_e64 v125, v217, v215
	v_cvt_pk_bf16_f32 v60, v70, v71
	v_cvt_pk_bf16_f32 v61, v72, v73
	v_cvt_pk_bf16_f32 v62, v74, v75
	v_cvt_pk_bf16_f32 v63, v76, v77
	v_mfma_f32_32x32x16_bf16 v[82:97], v[226:229], v[130:133], v[82:97]
	v_add_f32_e64 v124, v126, v124
	v_add_f32_e64 v125, v127, v125
	v_add_f32_e64 v126, v64, v80
	v_add_f32_e64 v127, v65, v81
	v_cvt_pk_bf16_f32 v64, v78, v79
	v_cvt_pk_bf16_f32 v65, v80, v81
	ds_read_b64_tr_b16 v[66:67], v203 offset:0
	ds_read_b64_tr_b16 v[68:69], v203 offset:0x400
	ds_read_b64_tr_b16 v[70:71], v203 offset:0x800
	s_waitcnt lgkmcnt(6)
	v_mfma_f32_32x32x16_bf16 v[98:113], v[230:233], v[146:149], v[98:113]
	ds_read_b64_tr_b16 v[72:73], v203 offset:0xc00
	ds_read_b64_tr_b16 v[74:75], v203 offset:0x1000
	ds_read_b64_tr_b16 v[76:77], v203 offset:0x1400
	ds_read_b64_tr_b16 v[78:79], v203 offset:0x1800
	ds_read_b64_tr_b16 v[80:81], v203 offset:0x1c00
	v_add_f32_e64 v124, v126, v124
	v_add_f32_e64 v125, v127, v125
	s_waitcnt lgkmcnt(9)
	v_mfma_f32_32x32x16_bf16 v[82:97], v[234:237], v[146:149], v[82:97]
	v_add_f32_e32 v124, v124, v125
	s_nop 0
	v_mov_b32_e32 v125, v124
	s_nop 1
	v_permlane32_swap_b32_e32 v124, v125
	v_mfma_f32_32x32x16_bf16 v[98:113], v[210:213], v[142:145], v[98:113]
	ds_read_b64_tr_b16 v[210:211], v203 offset:0x200
	ds_read_b64_tr_b16 v[212:213], v203 offset:0x600
	ds_read_b64_tr_b16 v[214:215], v203 offset:0xa00
	ds_read_b64_tr_b16 v[216:217], v203 offset:0xe00
	ds_read_b64_tr_b16 v[218:219], v203 offset:0x1200
	ds_read_b64_tr_b16 v[220:221], v203 offset:0x1600
	ds_read_b64_tr_b16 v[222:223], v203 offset:0x1a00
	s_waitcnt lgkmcnt(15)
	v_mfma_f32_32x32x16_bf16 v[82:97], v[238:241], v[142:145], v[82:97]
	ds_read_b64_tr_b16 v[224:225], v203 offset:0x1e00
	s_waitcnt lgkmcnt(4)
	v_mfma_f32_32x32x16_bf16 v[18:33], v[50:53], v[66:69], v[18:33]
	v_mfma_f32_32x32x16_bf16 v[2:17], v[50:53], v[210:213], v[2:17]
	s_nop 8
	v_max_f32_e32 v249, v99, v99
	v_max_f32_e32 v250, v98, v98
	v_max_f32_e32 v249, v250, v249
	v_max3_f32 v249, v249, v100, v101
	v_max3_f32 v249, v249, v102, v103
	v_max3_f32 v251, v249, v104, v105
	v_max3_f32 v251, v251, v106, v107
	v_exp_f32_e32 v50, v98
	v_exp_f32_e32 v51, v99
	v_exp_f32_e32 v52, v100
	v_exp_f32_e32 v53, v101
	v_mfma_f32_32x32x16_bf16 v[18:33], v[54:57], v[70:73], v[18:33]
	v_mfma_f32_32x32x16_bf16 v[2:17], v[54:57], v[214:217], v[2:17]
	v_max3_f32 v251, v251, v108, v109
	v_max3_f32 v251, v251, v110, v111
	v_max3_f32 v251, v251, v112, v113
	v_max3_f32 v251, v251, v82, v83
	v_max3_f32 v251, v251, v84, v85
	v_max3_f32 v251, v251, v86, v87
	v_max3_f32 v251, v251, v88, v89
	v_exp_f32_e32 v54, v102
	v_exp_f32_e32 v55, v103
	v_exp_f32_e32 v56, v104
	v_exp_f32_e32 v57, v105
	v_mfma_f32_32x32x16_bf16 v[18:33], v[58:61], v[74:77], v[18:33]
	s_waitcnt lgkmcnt(0)
	v_mfma_f32_32x32x16_bf16 v[2:17], v[58:61], v[218:221], v[2:17]
	v_max3_f32 v251, v251, v90, v91
	v_max3_f32 v251, v251, v92, v93
	v_max3_f32 v251, v251, v94, v95
	v_max3_f32 v251, v251, v96, v97
	v_mov_b32_e32 v252, v251
	s_nop 1
	v_permlane32_swap_b32_e32 v251, v252
	v_exp_f32_e32 v58, v106
	v_exp_f32_e32 v59, v107
	v_exp_f32_e32 v60, v108
	v_exp_f32_e32 v61, v109
	v_mfma_f32_32x32x16_bf16 v[18:33], v[62:65], v[78:81], v[18:33]
	v_mfma_f32_32x32x16_bf16 v[2:17], v[62:65], v[222:225], v[2:17]
	v_exp_f32_e32 v62, v110
	v_exp_f32_e32 v63, v111
	v_exp_f32_e32 v64, v112
	v_exp_f32_e32 v65, v113
	v_max_f32_e32 v252, v252, v252
	v_max_f32_e32 v251, v251, v251
	v_max_f32_e32 v126, v251, v252
	v_cmp_ge_f32_e32 vcc, s80, v126
	s_cmp_lg_u64 vcc, exec
	s_cselect_b64 s[6:7], -1, 0
	s_cbranch_scc1 .LBB0_2269
	v_mov_b32_e32 v209, 1.0
	v_mov_b32_e32 v210, v204
	s_branch .LBB0_2263

; template <bool FIRST> DEVI bool partialSM(f32x16& p0, f32x16& p1, float& m_reg, float& alpha) {
;     float pmax = p0[0];
; #pragma unroll
;     for (int r = 1; r < 16; ++r) pmax = fmaxf(pmax, p0[r]);
; #pragma unroll
;     for (int r = 0; r < 16; ++r) pmax = fmaxf(pmax, p1[r]);
;     { auto rr = __builtin_amdgcn_permlane32_swap(__float_as_uint(pmax), __float_as_uint(pmax), false, false);
;       pmax = fmaxf(__uint_as_float(rr[0]), __uint_as_float(rr[1])); }
;     if (FIRST) { m_reg = pmax; alpha = 1.f;
; #pragma unroll
;         for (int r = 0; r < 16; ++r) { p0[r] = __builtin_amdgcn_exp2f(p0[r] - pmax); p1[r] = p1[r] - pmax; }
;         return false;
;     } else if (__builtin_expect(__all(pmax <= ATT_THR), 1)) { alpha = 1.f;
; #pragma unroll
;         for (int r = 0; r < 16; ++r) p0[r] = __builtin_amdgcn_exp2f(p0[r]);
;         return false;
;     } else { const float d = fmaxf(pmax, 0.f); alpha = __builtin_amdgcn_exp2f(-d); m_reg += d;
; #pragma unroll
;         for (int r = 0; r < 16; ++r) { p0[r] = __builtin_amdgcn_exp2f(p0[r] - d); p1[r] = p1[r] - d; }
;         return true;
;     }
; }
; DEVI void finishSM(f32x16& p0, f32x16& p1, float alpha, float& l_reg, bf16x8& pa0, bf16x8& pa1, bf16x8& pa2, bf16x8& pa3) {
; #pragma unroll
;     for (int r = 0; r < 16; ++r) p1[r] = __builtin_amdgcn_exp2f(p1[r]);
;     f32x2 s2 = (f32x2){p0[0], p0[1]} + (f32x2){p1[0], p1[1]};
; #pragma unroll
;     for (int r = 2; r < 16; r += 2) s2 += (f32x2){p0[r], p0[r + 1]} + (f32x2){p1[r], p1[r + 1]};
;     float ps = s2[0] + s2[1];
;     { auto rr = __builtin_amdgcn_permlane32_swap(__float_as_uint(ps), __float_as_uint(ps), false, false);
;       ps = __uint_as_float(rr[0]) + __uint_as_float(rr[1]); }
;     l_reg = l_reg * alpha + ps;
;     ...
;     PK4(p0, 0, pa0); PK4(p0, 8, pa1); PK4(p1, 0, pa2); PK4(p1, 8, pa3);
;     ...
; }
; DEVI void qkt(f32x16& p0, f32x16& p1, const char* Kb, const bf16x8 (&qr)[6], int r32, int hi, const f32x16& cinit) {
; #pragma unroll
;     for (int d0 = 0; d0 < 6; ++d0) { const int cb = (d0 * 16 + hi * 8) * 2;
;         const bf16x8 k0 = *(const bf16x8*)(Kb + KSWZ(r32, cb)), k1 = *(const bf16x8*)(Kb + KSWZ(32 + r32, cb));
;         p0 = __builtin_amdgcn_mfma_f32_32x32x16_bf16(k0, qr[d0], d0 == 0 ? cinit : p0, 0, 0, 0);
;         p1 = __builtin_amdgcn_mfma_f32_32x32x16_bf16(k1, qr[d0], d0 == 0 ? cinit : p1, 0, 0, 0); }
; }
.LBB0_2266:
	s_mul_i32 s98, s61, 0x6000
	s_add_i32 s98, s96, s98
	s_lshl_b32 s99, s61, 14
	s_add_i32 s99, s97, s99
	s_mul_i32 s6, s2, 0x6000
	s_add_i32 s6, s6, 0
	v_add_u32_e32 v249, s6, v129
	v_lshl_add_u64 v[250:251], v[118:119], 0, s[12:13]
	s_mov_b32 m0, s98
	s_barrier
	ds_read_b128 v[234:237], v249
	ds_read_b128 v[212:215], v249 offset:6144
	global_load_lds_dwordx4 v[250:251], off
	v_exp_f32_e32 v82, v82
	s_waitcnt lgkmcnt(0)
	v_mfma_f32_32x32x16_bf16 v[98:113], v[234:237], v[150:153], v[34:49]
	v_add_u32_e32 v126, s6, v184
	v_lshl_add_u64 v[250:251], v[120:121], 0, s[12:13]
	s_add_i32 m0, s98, 0x2000
	v_exp_f32_e32 v83, v83
	v_exp_f32_e32 v84, v84
	global_load_lds_dwordx4 v[250:251], off
	v_exp_f32_e32 v85, v85
	v_exp_f32_e32 v86, v86
	v_exp_f32_e32 v87, v87
	v_exp_f32_e32 v88, v88
	v_mfma_f32_32x32x16_bf16 v[66:81], v[212:215], v[150:153], v[34:49]
	ds_read_b128 v[212:215], v126
	ds_read_b128 v[216:219], v126 offset:6144
	v_add_u32_e32 v126, s6, v185
	v_lshl_add_u64 v[250:251], v[122:123], 0, s[12:13]
	s_add_i32 m0, s98, 0x4000
	v_exp_f32_e32 v89, v89
	v_exp_f32_e32 v90, v90
	global_load_lds_dwordx4 v[250:251], off
	v_exp_f32_e32 v91, v91
	v_exp_f32_e32 v92, v92
	v_exp_f32_e32 v93, v93
	s_waitcnt lgkmcnt(0)
	v_mfma_f32_32x32x16_bf16 v[98:113], v[212:215], v[138:141], v[98:113]
	s_mov_b32 m0, s99
	v_exp_f32_e32 v94, v94
	v_exp_f32_e32 v95, v95
	v_lshl_add_u64 v[250:251], v[116:117], 0, s[40:41]
	global_load_lds_dwordx4 v[116:117], off
	s_add_i32 m0, s99, 0x2000
	v_exp_f32_e32 v96, v96
	v_exp_f32_e32 v97, v97
	v_add_u32_e32 v174, 0x2000, v203
	global_load_lds_dwordx4 v[250:251], off
	v_mfma_f32_32x32x16_bf16 v[66:81], v[216:219], v[138:141], v[66:81]
	ds_read_b128 v[212:215], v126
	ds_read_b128 v[216:219], v126 offset:6144
	v_add_u32_e32 v126, s6, v205
	s_waitcnt lgkmcnt(1)
	v_mfma_f32_32x32x16_bf16 v[98:113], v[212:215], v[134:137], v[98:113]
	ds_read_b128 v[212:215], v126
	ds_read_b128 v[220:223], v126 offset:6144
	v_add_u32_e32 v126, s6, v206
	s_waitcnt lgkmcnt(2)
	v_mfma_f32_32x32x16_bf16 v[66:81], v[216:219], v[134:137], v[66:81]
	ds_read_b128 v[216:219], v126
	ds_read_b128 v[224:227], v126 offset:6144
	v_add_u32_e32 v126, s6, v207
	ds_read_b128 v[228:231], v126
	ds_read_b128 v[232:235], v126 offset:6144
	v_add_f32_e32 v126, v50, v82
	v_add_f32_e32 v127, v51, v83
	v_cvt_pk_bf16_f32 v50, v50, v51
	v_cvt_pk_bf16_f32 v51, v52, v53
	s_waitcnt lgkmcnt(2)
	v_mfma_f32_32x32x16_bf16 v[98:113], v[212:215], v[130:133], v[98:113]
	v_add_f32_e64 v212, v52, v84
	v_add_f32_e64 v213, v53, v85
	v_cvt_pk_bf16_f32 v52, v54, v55
	v_cvt_pk_bf16_f32 v53, v56, v57
	v_add_f32_e64 v126, v212, v126
	v_add_f32_e64 v127, v213, v127
	v_add_f32_e64 v212, v54, v86
	v_add_f32_e64 v213, v55, v87
	v_cvt_pk_bf16_f32 v54, v58, v59
	v_mfma_f32_32x32x16_bf16 v[66:81], v[220:223], v[130:133], v[66:81]
	v_add_f32_e64 v126, v212, v126
	v_add_f32_e64 v127, v213, v127
	v_add_f32_e64 v212, v56, v88
	v_add_f32_e64 v213, v57, v89
	v_cvt_pk_bf16_f32 v55, v60, v61
	v_cvt_pk_bf16_f32 v56, v62, v63
	v_cvt_pk_bf16_f32 v57, v64, v65
	v_add_f32_e64 v126, v212, v126
	v_add_f32_e64 v127, v213, v127
	v_add_f32_e32 v212, v58, v90
	v_add_f32_e32 v213, v59, v91
	v_cvt_pk_bf16_f32 v58, v82, v83
	v_cvt_pk_bf16_f32 v59, v84, v85
	v_mfma_f32_32x32x16_bf16 v[98:113], v[216:219], v[146:149], v[98:113]
	v_add_f32_e64 v126, v212, v126
	v_add_f32_e64 v127, v213, v127
	v_add_f32_e64 v212, v60, v92
	v_add_f32_e64 v213, v61, v93
	v_cvt_pk_bf16_f32 v60, v86, v87
	v_cvt_pk_bf16_f32 v61, v88, v89
	v_add_f32_e64 v126, v212, v126
	v_add_f32_e64 v127, v213, v127
	v_add_f32_e32 v212, v62, v94
	v_add_f32_e32 v213, v63, v95
	v_cvt_pk_bf16_f32 v62, v90, v91
	v_cvt_pk_bf16_f32 v63, v92, v93
	v_mfma_f32_32x32x16_bf16 v[66:81], v[224:227], v[146:149], v[66:81]
	v_add_f32_e64 v126, v212, v126
	v_add_f32_e64 v127, v213, v127
	v_add_f32_e64 v212, v64, v96
	v_add_f32_e64 v213, v65, v97
	v_cvt_pk_bf16_f32 v64, v94, v95
	v_cvt_pk_bf16_f32 v65, v96, v97
	ds_read_b64_tr_b16 v[154:155], v174 offset:0
	ds_read_b64_tr_b16 v[156:157], v174 offset:0x400
	ds_read_b64_tr_b16 v[158:159], v174 offset:0x800
	ds_read_b64_tr_b16 v[160:161], v174 offset:0xc00
	ds_read_b64_tr_b16 v[162:163], v174 offset:0x1000
	ds_read_b64_tr_b16 v[164:165], v174 offset:0x1400
	ds_read_b64_tr_b16 v[166:167], v174 offset:0x1800
	ds_read_b64_tr_b16 v[168:169], v174 offset:0x1c00
	v_add_f32_e64 v126, v212, v126
	v_add_f32_e64 v127, v213, v127
	ds_read_b64_tr_b16 v[212:213], v174 offset:0x200
	ds_read_b64_tr_b16 v[214:215], v174 offset:0x600
	ds_read_b64_tr_b16 v[216:217], v174 offset:0xa00
	s_waitcnt lgkmcnt(12)
	v_mfma_f32_32x32x16_bf16 v[98:113], v[228:231], v[142:145], v[98:113]
	ds_read_b64_tr_b16 v[218:219], v174 offset:0xe00
	ds_read_b64_tr_b16 v[220:221], v174 offset:0x1200
	ds_read_b64_tr_b16 v[222:223], v174 offset:0x1600
	ds_read_b64_tr_b16 v[224:225], v174 offset:0x1a00
	ds_read_b64_tr_b16 v[226:227], v174 offset:0x1e00
	v_add_f32_e32 v126, v126, v127
	s_waitcnt lgkmcnt(6)
	v_mfma_f32_32x32x16_bf16 v[66:81], v[232:235], v[142:145], v[66:81]
	v_mov_b32_e32 v127, v126
	s_nop 1
	v_permlane32_swap_b32_e32 v126, v127
	v_mfma_f32_32x32x16_bf16 v[18:33], v[50:53], v[154:157], v[18:33]
	v_mfma_f32_32x32x16_bf16 v[2:17], v[50:53], v[212:215], v[2:17]
	s_nop 4
	v_max_f32_e32 v249, v99, v99
	v_max_f32_e32 v250, v98, v98
	v_max_f32_e32 v249, v250, v249
	v_max3_f32 v249, v249, v100, v101
	v_max3_f32 v249, v249, v102, v103
	v_max3_f32 v251, v249, v104, v105
	v_max3_f32 v251, v251, v106, v107
	v_exp_f32_e32 v50, v98
	v_exp_f32_e32 v51, v99
	v_exp_f32_e32 v52, v100
	v_exp_f32_e32 v53, v101
	v_mfma_f32_32x32x16_bf16 v[18:33], v[54:57], v[158:161], v[18:33]
	s_waitcnt lgkmcnt(2)
	v_mfma_f32_32x32x16_bf16 v[2:17], v[54:57], v[216:219], v[2:17]
	v_max3_f32 v251, v251, v108, v109
	v_max3_f32 v251, v251, v110, v111
	v_max3_f32 v251, v251, v112, v113
	v_max3_f32 v251, v251, v66, v67
	v_max3_f32 v251, v251, v68, v69
	v_max3_f32 v251, v251, v70, v71
	v_max3_f32 v251, v251, v72, v73
	v_exp_f32_e32 v54, v102
	v_exp_f32_e32 v55, v103
	v_exp_f32_e32 v56, v104
	v_exp_f32_e32 v57, v105
	v_mfma_f32_32x32x16_bf16 v[18:33], v[58:61], v[162:165], v[18:33]
	v_mfma_f32_32x32x16_bf16 v[2:17], v[58:61], v[220:223], v[2:17]
	v_max3_f32 v251, v251, v74, v75
	v_max3_f32 v251, v251, v76, v77
	v_max3_f32 v251, v251, v78, v79
	v_max3_f32 v251, v251, v80, v81
	v_mov_b32_e32 v252, v251
	s_nop 1
	v_permlane32_swap_b32_e32 v251, v252
	v_exp_f32_e32 v58, v106
	v_exp_f32_e32 v59, v107
	v_exp_f32_e32 v60, v108
	v_exp_f32_e32 v61, v109
	v_mfma_f32_32x32x16_bf16 v[18:33], v[62:65], v[166:169], v[18:33]
	s_waitcnt lgkmcnt(0)
	v_mfma_f32_32x32x16_bf16 v[2:17], v[62:65], v[224:227], v[2:17]
	v_exp_f32_e32 v62, v110
	v_exp_f32_e32 v63, v111
	v_exp_f32_e32 v64, v112
	v_exp_f32_e32 v65, v113
	v_max_f32_e32 v252, v252, v252
	v_max_f32_e32 v251, v251, v251
	v_max_f32_e32 v174, v251, v252
	v_cmp_ge_f32_e32 vcc, s80, v174
	s_cmp_lg_u64 vcc, exec
	s_cselect_b64 s[6:7], -1, 0
	s_cbranch_scc1 .LBB0_2275
	v_mov_b32_e32 v203, 1.0
	v_mov_b32_e32 v204, v210
	s_branch .LBB0_2280
